# v90 + grid barrier: the last XCD leader bumps every XCD's local release word itself right after the cross-XCD generation (one poll + one atomic hop less for the other XCDs); leaders no longer relay
# baseline (speedup 1.0000x reference)
.LBB0_404:
	s_or_b64 exec, exec, s[36:37]
	s_and_saveexec_b64 s[36:37], s[26:27]
	s_cbranch_execz .LBB0_406
	global_atomic_add v[2:3], v236, off
	v_readlane_b32 s4, v254, 7
	v_readlane_b32 s5, v254, 8
	s_getreg_b32 s3, hwreg(HW_REG_XCC_ID, 0, 4)
	s_lshl_b32 s3, s3, 8
	s_nop 4
	s_sub_u32 s4, s4, s3
	s_subb_u32 s5, s5, 0
	global_atomic_add v67, v236, s[4:5]
	global_atomic_add v67, v236, s[4:5] offset:256
	global_atomic_add v67, v236, s[4:5] offset:512
	global_atomic_add v67, v236, s[4:5] offset:768
	global_atomic_add v67, v236, s[4:5] offset:1024
	global_atomic_add v67, v236, s[4:5] offset:1280
	global_atomic_add v67, v236, s[4:5] offset:1536
	global_atomic_add v67, v236, s[4:5] offset:1792
	global_atomic_add v67, v236, s[4:5] offset:2048
	global_atomic_add v67, v236, s[4:5] offset:2304
	global_atomic_add v67, v236, s[4:5] offset:2560
	global_atomic_add v67, v236, s[4:5] offset:2816
	global_atomic_add v67, v236, s[4:5] offset:3072
	global_atomic_add v67, v236, s[4:5] offset:3328
	global_atomic_add v67, v236, s[4:5] offset:3584
	global_atomic_add v67, v236, s[4:5] offset:3840
.LBB0_406:
	s_or_b64 exec, exec, s[36:37]
	s_mov_b64 s[26:27], exec
	v_mbcnt_lo_u32_b32 v2, s26, 0
	v_mbcnt_hi_u32_b32 v2, s27, v2
	v_cmp_eq_u32_e32 vcc, 0, v2
	s_waitcnt vmcnt(0)
	s_and_saveexec_b64 s[36:37], vcc
	s_cbranch_execz .LBB0_408
	s_bcnt1_i32_b64 s3, s[26:27]
	v_readlane_b32 s4, v254, 7
	v_mov_b32_e32 v2, s3
	v_readlane_b32 s5, v254, 8
	s_nop 4
.LBB0_408:
	s_or_b64 exec, exec, s[36:37]
	s_waitcnt vmcnt(0)

.LBB0_785:
	s_or_b64 exec, exec, s[36:37]
	s_mov_b64 s[26:27], exec
	v_mbcnt_lo_u32_b32 v2, s26, 0
	v_mbcnt_hi_u32_b32 v2, s27, v2
	v_cmp_eq_u32_e32 vcc, 0, v2
	s_waitcnt vmcnt(0)
	s_and_saveexec_b64 s[36:37], vcc
	s_cbranch_execz .LBB0_787
	s_bcnt1_i32_b64 s2, s[26:27]
	v_mov_b32_e32 v2, s2
	v_readlane_b32 s2, v254, 7
	v_readlane_b32 s3, v254, 8
	s_nop 4
.LBB0_787:
	s_or_b64 exec, exec, s[36:37]
	s_waitcnt vmcnt(0)

.LBB0_895:
	s_or_b64 exec, exec, s[36:37]
	s_mov_b64 s[26:27], exec
	v_mbcnt_lo_u32_b32 v2, s26, 0
	v_mbcnt_hi_u32_b32 v2, s27, v2
	v_cmp_eq_u32_e32 vcc, 0, v2
	s_waitcnt vmcnt(0)
	s_and_saveexec_b64 s[36:37], vcc
	s_cbranch_execz .LBB0_897
	s_bcnt1_i32_b64 s2, s[26:27]
	v_mov_b32_e32 v2, s2
	v_readlane_b32 s2, v254, 7
	v_readlane_b32 s3, v254, 8
	s_nop 4
.LBB0_897:
	s_or_b64 exec, exec, s[36:37]
	s_waitcnt vmcnt(0)

.LBB0_984:
	s_or_b64 exec, exec, s[36:37]
	s_mov_b64 s[26:27], exec
	v_mbcnt_lo_u32_b32 v2, s26, 0
	v_mbcnt_hi_u32_b32 v2, s27, v2
	v_cmp_eq_u32_e32 vcc, 0, v2
	s_waitcnt vmcnt(0)
	s_and_saveexec_b64 s[36:37], vcc
	s_cbranch_execz .LBB0_986
	s_bcnt1_i32_b64 s3, s[26:27]
	v_readlane_b32 s4, v254, 7
	v_mov_b32_e32 v2, s3
	v_readlane_b32 s5, v254, 8
	s_nop 4
.LBB0_986:
	s_or_b64 exec, exec, s[36:37]
	s_waitcnt vmcnt(0)

.LBB0_1122:
	s_or_b64 exec, exec, s[36:37]
	s_mov_b64 s[26:27], exec
	v_mbcnt_lo_u32_b32 v2, s26, 0
	v_mbcnt_hi_u32_b32 v2, s27, v2
	v_cmp_eq_u32_e32 vcc, 0, v2
	s_waitcnt vmcnt(0)
	s_and_saveexec_b64 s[36:37], vcc
	s_cbranch_execz .LBB0_1124
	s_bcnt1_i32_b64 s2, s[26:27]
	v_mov_b32_e32 v2, s2
	v_readlane_b32 s2, v254, 7
	v_readlane_b32 s3, v254, 8
	s_nop 4
.LBB0_1124:
	s_or_b64 exec, exec, s[36:37]
	s_waitcnt vmcnt(0)

.LBB0_1190:
	s_or_b64 exec, exec, s[36:37]
	s_mov_b64 s[26:27], exec
	v_mbcnt_lo_u32_b32 v2, s26, 0
	v_mbcnt_hi_u32_b32 v2, s27, v2
	v_cmp_eq_u32_e32 vcc, 0, v2
	s_waitcnt vmcnt(0)
	s_and_saveexec_b64 s[36:37], vcc
	s_cbranch_execz .LBB0_1192
	s_bcnt1_i32_b64 s3, s[26:27]
	v_readlane_b32 s4, v254, 7
	v_mov_b32_e32 v2, s3
	v_readlane_b32 s5, v254, 8
	s_nop 4
.LBB0_1192:
	s_or_b64 exec, exec, s[36:37]
	s_waitcnt vmcnt(0)

.LBB0_1448:
	s_or_b64 exec, exec, s[36:37]
	s_mov_b64 s[26:27], exec
	v_mbcnt_lo_u32_b32 v2, s26, 0
	v_mbcnt_hi_u32_b32 v2, s27, v2
	v_cmp_eq_u32_e32 vcc, 0, v2
	s_waitcnt vmcnt(0)
	s_and_saveexec_b64 s[36:37], vcc
	s_cbranch_execz .LBB0_1450
	s_bcnt1_i32_b64 s3, s[26:27]
	v_readlane_b32 s4, v254, 7
	v_mov_b32_e32 v2, s3
	v_readlane_b32 s5, v254, 8
	s_nop 4
.LBB0_1450:
	s_or_b64 exec, exec, s[36:37]
	s_waitcnt vmcnt(0)

.LBB0_1665:
	s_or_b64 exec, exec, s[36:37]
	s_mov_b64 s[26:27], exec
	v_mbcnt_lo_u32_b32 v2, s26, 0
	v_mbcnt_hi_u32_b32 v2, s27, v2
	v_cmp_eq_u32_e32 vcc, 0, v2
	s_waitcnt vmcnt(0)
	s_and_saveexec_b64 s[36:37], vcc
	s_cbranch_execz .LBB0_1667
	s_bcnt1_i32_b64 s3, s[26:27]
	v_readlane_b32 s4, v254, 7
	v_mov_b32_e32 v2, s3
	v_readlane_b32 s5, v254, 8
	s_nop 4
.LBB0_1667:
	s_or_b64 exec, exec, s[36:37]
	s_waitcnt vmcnt(0)

.LBB0_1797:
	s_bcnt1_i32_b64 s2, s[26:27]
	v_mov_b32_e32 v2, s2
	v_readlane_b32 s2, v254, 7
	v_readlane_b32 s3, v254, 8
	s_nop 4
	s_getpc_b64 s[98:99]
